# guconv2 + nt (streaming) hint on the f32 weight piece loads in the gate/up K loop
# speedup vs baseline: 1.0045x; 1.0045x over previous
.LBB0_689:
	s_cmp_lg_u32 s39, 4
	s_cselect_b64 s[70:71], -1, 0
	s_add_u32 s4, s58, s64
	v_add_u32_e32 v2, 0x10000, v201
	v_add_u32_e32 v14, 0x14000, v201
	s_addc_u32 s5, s59, s65
	ds_read_b128 v[18:21], v2
	ds_read_b128 v[22:25], v2 offset:1024
	ds_read_b128 v[26:29], v2 offset:2048
	ds_read_b128 v[30:33], v2 offset:3072
	ds_read_b128 v[2:5], v14
	ds_read_b128 v[6:9], v14 offset:1024
	ds_read_b128 v[10:13], v14 offset:2048
	ds_read_b128 v[14:17], v14 offset:3072
	s_add_u32 s4, s4, 0xa3100100
	s_addc_u32 s5, s5, -1
	s_cmp_eq_u32 s39, 4
	s_cselect_b64 s[68:69], -1, 0
	s_and_b64 vcc, s[68:69], exec
	s_cselect_b32 s67, s17, s5
	s_cselect_b32 s66, s19, s4
	ds_read_b128 v[34:37], v202
	ds_read_b128 v[38:41], v202 offset:1024
	ds_read_b128 v[42:45], v202 offset:2048
	ds_read_b128 v[46:49], v202 offset:3072
	ds_read_b128 v[50:53], v202 offset:4096
	ds_read_b128 v[54:57], v202 offset:5120
	ds_read_b128 v[58:61], v202 offset:6144
	ds_read_b128 v[62:65], v202 offset:7168
	s_add_u32 s4, s12, s64
	s_addc_u32 s5, s13, s65
	s_add_u32 s4, s4, 0x80
	s_addc_u32 s5, s5, 0
	s_mov_b32 s91, m0
	s_mov_b32 m0, s82
	s_nop 0
	global_load_lds_dwordx4 v216, s[4:5]
	s_mov_b32 m0, s91
	s_add_i32 s91, s35, 0xe000
	s_mov_b32 s92, m0
	s_mov_b32 m0, s91
	s_nop 0
	global_load_lds_dwordx4 v217, s[4:5]
	s_mov_b32 m0, s92
	s_add_i32 s100, s39, 2
	s_lshl_b32 s100, s100, 13
	s_and_b32 s101, s98, 15
	s_lshl_b32 s101, s101, 8
	s_add_u32 s100, s100, s101
	s_mov_b32 s101, 0
	v_lshl_add_u64 v[240:241], v[250:251], 0, s[100:101]
	global_load_dwordx4 v[224:227], v[240:241], off nt
	s_waitcnt vmcnt(9)
	s_waitcnt lgkmcnt(0)
	s_barrier
	s_setprio 1
	s_waitcnt lgkmcnt(0)
	v_mfma_f32_16x16x128_f8f6f4 v[190:193], v[18:25], v[34:41], v[190:193]
	v_mfma_f32_16x16x128_f8f6f4 v[186:189], v[26:33], v[34:41], v[186:189]
	v_mfma_f32_16x16x128_f8f6f4 v[182:185], v[18:25], v[42:49], v[182:185]
	v_mfma_f32_16x16x128_f8f6f4 v[178:181], v[26:33], v[42:49], v[178:181]
	v_mfma_f32_16x16x128_f8f6f4 v[174:177], v[18:25], v[50:57], v[174:177]
	v_mfma_f32_16x16x128_f8f6f4 v[170:173], v[26:33], v[50:57], v[170:173]
	v_mfma_f32_16x16x128_f8f6f4 v[166:169], v[18:25], v[58:65], v[166:169]
	v_mfma_f32_16x16x128_f8f6f4 v[162:165], v[26:33], v[58:65], v[162:165]
	s_setprio 0
	s_setprio 1
	v_mfma_f32_16x16x128_f8f6f4 v[158:161], v[2:9], v[34:41], v[158:161]
	v_mfma_f32_16x16x128_f8f6f4 v[154:157], v[10:17], v[34:41], v[154:157]
	v_mfma_f32_16x16x128_f8f6f4 v[150:153], v[2:9], v[42:49], v[150:153]
	v_mfma_f32_16x16x128_f8f6f4 v[146:149], v[10:17], v[42:49], v[146:149]
	v_mfma_f32_16x16x128_f8f6f4 v[142:145], v[2:9], v[50:57], v[142:145]
	v_mfma_f32_16x16x128_f8f6f4 v[138:141], v[10:17], v[50:57], v[138:141]
	v_mfma_f32_16x16x128_f8f6f4 v[134:137], v[2:9], v[58:65], v[134:137]
	v_mfma_f32_16x16x128_f8f6f4 v[130:133], v[10:17], v[58:65], v[130:133]
	s_setprio 0
	s_barrier
	ds_read_b128 v[58:61], v202 offset:16384
	ds_read_b128 v[62:65], v202 offset:17408
	ds_read_b128 v[50:53], v202 offset:18432
	ds_read_b128 v[54:57], v202 offset:19456
	ds_read_b128 v[42:45], v202 offset:20480
	ds_read_b128 v[46:49], v202 offset:21504
	ds_read_b128 v[34:37], v202 offset:22528
	ds_read_b128 v[38:41], v202 offset:23552
	s_mov_b32 s4, m0
	s_mov_b32 m0, s53
	s_nop 0
	global_load_lds_dwordx4 v196, s[66:67]
	s_mov_b32 m0, s4
	s_nop 0
	s_mov_b32 s4, m0
	s_mov_b32 m0, s55
	s_nop 0
	global_load_lds_dwordx4 v197, s[66:67]
	s_mov_b32 m0, s4
	s_add_u32 s4, s66, 0x20000
	s_addc_u32 s5, s67, 0
	s_mov_b32 s91, m0
	s_mov_b32 m0, s57
	s_nop 0
	global_load_lds_dwordx4 v196, s[4:5]
	s_mov_b32 m0, s91
	s_nop 0
	s_mov_b32 s91, m0
	s_mov_b32 m0, s72
	s_nop 0
	global_load_lds_dwordx4 v197, s[4:5]
	s_mov_b32 m0, s91
	s_mov_b64 s[4:5], -1
	s_cbranch_vccnz .LBB0_691
	s_add_u32 s4, s40, s64
	s_addc_u32 s5, s41, s65
	s_add_u32 s4, s4, 0xa3100100
	s_addc_u32 s5, s5, -1
	s_mov_b32 s91, m0
	s_mov_b32 m0, s35
	s_nop 0
	global_load_lds_dwordx4 v218, s[4:5]
	s_mov_b32 m0, s91
	s_nop 0
	s_mov_b32 s91, m0
	s_mov_b32 m0, s73
	s_nop 0
	global_load_lds_dwordx4 v215, s[4:5]
	s_mov_b32 m0, s91
	s_mov_b64 s[4:5], 0
